# s20 + P5 cross-trip prefetch: next trip's 16 row loads issued at the top of a trip into spare VGPRs (no exposed load round trip per trip)
# baseline (speedup 1.0000x reference)
; __global__ void __launch_bounds__(NTHREADS, 2) fwd(Args args) {
;     ...
;         const int c0 = 16 * lane; float ng[16];
; #pragma unroll
;         for (int j = 0; j < 4; ++j) { const f32x4 g4 = *(const f32x4*)(gla_norm_g + ((c0 + 4 * j) & 255)); ng[4 * j] = g4.x; ng[4 * j + 1] = g4.y; ng[4 * j + 2] = g4.z; ng[4 * j + 3] = g4.w; }
;         for (int m0 = gw; m0 < T; m0 += 2 * NGWc) {
;             u32x4 ra[2][2], rb[2][2], ri[2][2]; u32x4 rg[2][2];
; #pragma unroll
;             for (int t2 = 0; t2 < 2; ++t2) { const int m = (m0 + t2 * NGWc) < T ? m0 + t2 * NGWc : m0;
; #pragma unroll
;                 for (int j = 0; j < 2; ++j) { ra[t2][j] = *(const u32x4*)(OF + (size_t)m * 1024 + c0 + 8 * j); rb[t2][j] = *(const u32x4*)(OB + (size_t)m * 1024 + c0 + 8 * j); ri[t2][j] = *(const u32x4*)(OI + (size_t)m * 1024 + c0 + 8 * j); }
;                 rg[t2][0] = *(const u32x4*)(P + (size_t)m * NP + C_GO + c0); rg[t2][1] = *(const u32x4*)(P + (size_t)m * NP + C_GO + c0 + 8); }
.LBB0_595:
	s_add_u32 s0, s88, 0x47600000
	s_addc_u32 s1, s89, 0
	s_xor_b64 s[2:3], s[4:5], -1
	s_nor_b64 s[2:3], s[2:3], s[70:71]
	s_cmpk_lt_i32 s50, 0x4000
	s_cselect_b64 s[18:19], -1, 0
	s_and_b64 s[2:3], s[2:3], s[18:19]
	s_andn2_b64 vcc, exec, s[2:3]
	s_cbranch_vccnz .LBB0_600
	s_waitcnt vmcnt(0)
	v_lshlrev_b32_e32 v2, 6, v220
	v_and_b32_e32 v14, 0x3c0, v2
	global_load_dwordx4 v[2:5], v14, s[54:55]
	global_load_dwordx4 v[6:9], v14, s[54:55] offset:16
	global_load_dwordx4 v[10:13], v14, s[54:55] offset:32
	s_nop 0
	global_load_dwordx4 v[14:17], v14, s[54:55] offset:48
	v_mbcnt_lo_u32_b32 v19, -1, 0
	v_mbcnt_hi_u32_b32 v19, -1, v19
	v_and_b32_e32 v21, 64, v19
	v_xor_b32_e32 v20, 1, v19
	v_add_u32_e32 v21, 64, v21
	v_cmp_lt_i32_e32 vcc, v20, v21
	v_readlane_b32 s6, v246, 10
	v_readlane_b32 s2, v246, 23
	v_cndmask_b32_e32 v20, v19, v20, vcc
	v_lshlrev_b32_e32 v82, 2, v20
	v_xor_b32_e32 v20, 2, v19
	v_cmp_lt_i32_e32 vcc, v20, v21
	v_lshlrev_b32_e32 v18, 4, v220
	v_mov_b32_e32 v59, 0
	v_cndmask_b32_e32 v20, v19, v20, vcc
	v_lshlrev_b32_e32 v83, 2, v20
	v_xor_b32_e32 v20, 4, v19
	v_cmp_lt_i32_e32 vcc, v20, v21
	v_lshlrev_b32_e32 v58, 5, v220
	s_lshl_b32 s3, s6, 4
	v_cndmask_b32_e32 v20, v19, v20, vcc
	v_lshlrev_b32_e32 v84, 2, v20
	v_xor_b32_e32 v20, 8, v19
	v_cmp_lt_i32_e32 vcc, v20, v21
	s_lshl_b32 s2, s2, 3
	v_lshl_add_u64 v[60:61], s[12:13], 0, v[58:59]
	v_cndmask_b32_e32 v19, v19, v20, vcc
	v_lshl_add_u64 v[62:63], s[10:11], 0, v[58:59]
	v_lshl_add_u64 v[64:65], s[68:69], 0, v[58:59]
	v_lshlrev_b32_e32 v85, 2, v19
	v_lshl_add_u64 v[66:67], s[0:1], 0, v[58:59]
	s_addk_i32 s3, 0xfe00
	v_lshlrev_b32_e32 v58, 1, v18
	s_mov_b64 s[8:9], 0x2000
	s_movk_i32 s20, 0x2000
	v_mov_b32_e32 v86, 0x358637bd
	s_mov_b32 s21, 0xf800000
	v_mov_b32_e32 v87, 0x260
	s_mov_b32 s10, s50
	v_readlane_b32 s7, v246, 11
	s_mov_b32 s22, s10
	s_ashr_i32 s23, s22, 31
	s_lshl_b64 s[24:25], s[22:23], 11
	s_mul_hi_i32 s7, s22, 0x2800
	s_mul_i32 s6, s22, 0x2800
	s_add_u32 s6, s62, s6
	s_addc_u32 s7, s63, s7
	s_add_u32 s6, s6, 0x2000
	s_addc_u32 s7, s7, 0
	v_lshl_add_u64 v[200:201], v[60:61], 0, s[24:25]
	global_load_dwordx4 v[126:129], v[200:201], off offset:16
	s_nop 0
	global_load_dwordx4 v[200:203], v[200:201], off
	s_nop 0
	v_lshl_add_u64 v[196:197], v[62:63], 0, s[24:25]
	global_load_dwordx4 v[130:133], v[196:197], off offset:16
	s_nop 0
	global_load_dwordx4 v[196:199], v[196:197], off
	s_nop 0
	v_lshl_add_u64 v[142:143], v[64:65], 0, s[24:25]
	global_load_dwordx4 v[134:137], v[142:143], off offset:16
	s_nop 0
	global_load_dwordx4 v[142:145], v[142:143], off
	s_nop 0
	v_lshl_add_u64 v[204:205], s[6:7], 0, v[58:59]
	global_load_dwordx4 v[138:141], v[204:205], off offset:16
	s_nop 0
	global_load_dwordx4 v[204:207], v[204:205], off
	s_nop 0
	s_add_i32 s13, s22, s2
	s_cmpk_lt_i32 s13, 0x4000
	s_cselect_b32 s22, s13, s22
	s_ashr_i32 s23, s22, 31
	s_lshl_b64 s[24:25], s[22:23], 11
	s_mul_hi_i32 s7, s22, 0x2800
	s_mul_i32 s6, s22, 0x2800
	s_add_u32 s6, s62, s6
	s_addc_u32 s7, s63, s7
	s_add_u32 s6, s6, 0x2000
	s_addc_u32 s7, s7, 0
	v_lshl_add_u64 v[212:213], v[60:61], 0, s[24:25]
	global_load_dwordx4 v[208:211], v[212:213], off offset:16
	s_nop 0
	global_load_dwordx4 v[212:215], v[212:213], off
	s_nop 0
	v_lshl_add_u64 v[224:225], v[62:63], 0, s[24:25]
	global_load_dwordx4 v[216:219], v[224:225], off offset:16
	s_nop 0
	global_load_dwordx4 v[224:227], v[224:225], off
	s_nop 0
	v_lshl_add_u64 v[232:233], v[64:65], 0, s[24:25]
	global_load_dwordx4 v[228:231], v[232:233], off offset:16
	s_nop 0
	global_load_dwordx4 v[232:235], v[232:233], off
	s_nop 0
	v_lshl_add_u64 v[236:237], s[6:7], 0, v[58:59]
	global_load_dwordx4 v[240:243], v[236:237], off offset:16
	s_nop 0
	global_load_dwordx4 v[236:239], v[236:237], off
	s_nop 0
	s_waitcnt vmcnt(0)
	s_branch .Lmy_p5_entry

; __global__ void __launch_bounds__(NTHREADS, 2) fwd(Args args) {
;     ...
;         for (int m0 = gw; m0 < T; m0 += 2 * NGWc) {
;             u32x4 ra[2][2], rb[2][2], ri[2][2]; u32x4 rg[2][2];
; #pragma unroll
;             for (int t2 = 0; t2 < 2; ++t2) { const int m = (m0 + t2 * NGWc) < T ? m0 + t2 * NGWc : m0;
; #pragma unroll
;                 for (int j = 0; j < 2; ++j) { ra[t2][j] = *(const u32x4*)(OF + (size_t)m * 1024 + c0 + 8 * j); rb[t2][j] = *(const u32x4*)(OB + (size_t)m * 1024 + c0 + 8 * j); ri[t2][j] = *(const u32x4*)(OI + (size_t)m * 1024 + c0 + 8 * j); }
;                 rg[t2][0] = *(const u32x4*)(P + (size_t)m * NP + C_GO + c0); rg[t2][1] = *(const u32x4*)(P + (size_t)m * NP + C_GO + c0 + 8); }
; #pragma unroll
;             for (int t2 = 0; t2 < 2; ++t2) { const int m = m0 + t2 * NGWc; if (m >= T) break;
;                 float o[16];
; #pragma unroll
;                 for (int j = 0; j < 2; ++j) { const unsigned a[4] = {ra[t2][j].x, ra[t2][j].y, ra[t2][j].z, ra[t2][j].w}, b2[4] = {rb[t2][j].x, rb[t2][j].y, rb[t2][j].z, rb[t2][j].w}, i3[4] = {ri[t2][j].x, ri[t2][j].y, ri[t2][j].z, ri[t2][j].w};
; #pragma unroll
;                     for (int q = 0; q < 4; ++q) { o[8 * j + 2 * q] = (bflo(a[q]) + bflo(b2[q])) + bflo(i3[q]); o[8 * j + 2 * q + 1] = (bfhi(a[q]) + bfhi(b2[q])) + bfhi(i3[q]); } }
;                 float ss = 0.f;
; #pragma unroll
;                 for (int j = 0; j < 16; ++j) ss += o[j] * o[j];
;                 ss += __shfl_xor(ss, 1); ss += __shfl_xor(ss, 2); ss += __shfl_xor(ss, 4); ss += __shfl_xor(ss, 8);
;                 const float rms = 1.f / sqrtf(ss * (1.f / 256.f) + RMS_EPS);
;                 const unsigned gw8[8] = {rg[t2][0].x, rg[t2][0].y, rg[t2][0].z, rg[t2][0].w, rg[t2][1].x, rg[t2][1].y, rg[t2][1].z, rg[t2][1].w};
;                 float r[16];
; #pragma unroll
;                 for (int j = 0; j < 8; ++j) { const float g0 = bflo(gw8[j]), g1 = bfhi(gw8[j]);
;                     r[2 * j] = o[2 * j] * rms * ng[2 * j] * g0 * __builtin_amdgcn_rcpf(1.f + __expf(-g0)); r[2 * j + 1] = o[2 * j + 1] * rms * ng[2 * j + 1] * g1 * __builtin_amdgcn_rcpf(1.f + __expf(-g1)); }
.LBB0_598:
	s_waitcnt vmcnt(4)
.Lmy_p5_entry:
	s_add_i32 s12, s2, s10
	s_ashr_i32 s11, s10, 31
	s_lshl_b64 s[14:15], s[10:11], 12
	v_mov_b64_e32 v[88:89], v[126:127]
	v_mov_b64_e32 v[90:91], v[128:129]
	v_mov_b64_e32 v[92:93], v[130:131]
	v_mov_b64_e32 v[94:95], v[132:133]
	v_mov_b64_e32 v[96:97], v[134:135]
	v_mov_b64_e32 v[98:99], v[136:137]
	v_mov_b64_e32 v[50:51], v[138:139]
	v_mov_b64_e32 v[52:53], v[140:141]
	v_mov_b64_e32 v[100:101], v[142:143]
	v_mov_b64_e32 v[102:103], v[144:145]
	v_mov_b64_e32 v[104:105], v[196:197]
	v_mov_b64_e32 v[106:107], v[198:199]
	v_mov_b64_e32 v[108:109], v[200:201]
	v_mov_b64_e32 v[110:111], v[202:203]
	v_mov_b64_e32 v[54:55], v[204:205]
	v_mov_b64_e32 v[56:57], v[206:207]
	v_mov_b64_e32 v[46:47], v[208:209]
	v_mov_b64_e32 v[48:49], v[210:211]
	v_mov_b64_e32 v[34:35], v[212:213]
	v_mov_b64_e32 v[36:37], v[214:215]
	v_mov_b64_e32 v[42:43], v[216:217]
	v_mov_b64_e32 v[44:45], v[218:219]
	v_mov_b64_e32 v[30:31], v[224:225]
	v_mov_b64_e32 v[32:33], v[226:227]
	v_mov_b64_e32 v[38:39], v[228:229]
	v_mov_b64_e32 v[40:41], v[230:231]
	v_mov_b64_e32 v[26:27], v[232:233]
	v_mov_b64_e32 v[28:29], v[234:235]
	v_mov_b64_e32 v[22:23], v[236:237]
	v_mov_b64_e32 v[24:25], v[238:239]
	v_mov_b64_e32 v[18:19], v[240:241]
	v_mov_b64_e32 v[20:21], v[242:243]
	s_add_i32 s22, s10, s3
	s_cmpk_lt_i32 s22, 0x4000
	s_cbranch_scc0 .Lmy_p5_noload
	s_ashr_i32 s23, s22, 31
	s_lshl_b64 s[24:25], s[22:23], 11
	s_mul_hi_i32 s7, s22, 0x2800
	s_mul_i32 s6, s22, 0x2800
	s_add_u32 s6, s62, s6
	s_addc_u32 s7, s63, s7
	s_add_u32 s6, s6, 0x2000
	s_addc_u32 s7, s7, 0
	v_lshl_add_u64 v[200:201], v[60:61], 0, s[24:25]
	global_load_dwordx4 v[126:129], v[200:201], off offset:16
	s_nop 0
	global_load_dwordx4 v[200:203], v[200:201], off
	s_nop 0
	v_lshl_add_u64 v[196:197], v[62:63], 0, s[24:25]
	global_load_dwordx4 v[130:133], v[196:197], off offset:16
	s_nop 0
	global_load_dwordx4 v[196:199], v[196:197], off
	s_nop 0
	v_lshl_add_u64 v[142:143], v[64:65], 0, s[24:25]
	global_load_dwordx4 v[134:137], v[142:143], off offset:16
	s_nop 0
	global_load_dwordx4 v[142:145], v[142:143], off
	s_nop 0
	v_lshl_add_u64 v[204:205], s[6:7], 0, v[58:59]
	global_load_dwordx4 v[138:141], v[204:205], off offset:16
	s_nop 0
	global_load_dwordx4 v[204:207], v[204:205], off
	s_nop 0
	s_add_i32 s13, s22, s2
	s_cmpk_lt_i32 s13, 0x4000
	s_cselect_b32 s22, s13, s22
	s_ashr_i32 s23, s22, 31
	s_lshl_b64 s[24:25], s[22:23], 11
	s_mul_hi_i32 s7, s22, 0x2800
	s_mul_i32 s6, s22, 0x2800
	s_add_u32 s6, s62, s6
	s_addc_u32 s7, s63, s7
	s_add_u32 s6, s6, 0x2000
	s_addc_u32 s7, s7, 0
	v_lshl_add_u64 v[212:213], v[60:61], 0, s[24:25]
	global_load_dwordx4 v[208:211], v[212:213], off offset:16
	s_nop 0
	global_load_dwordx4 v[212:215], v[212:213], off
	s_nop 0
	v_lshl_add_u64 v[224:225], v[62:63], 0, s[24:25]
	global_load_dwordx4 v[216:219], v[224:225], off offset:16
	s_nop 0
	global_load_dwordx4 v[224:227], v[224:225], off
	s_nop 0
	v_lshl_add_u64 v[232:233], v[64:65], 0, s[24:25]
	global_load_dwordx4 v[228:231], v[232:233], off offset:16
	s_nop 0
	global_load_dwordx4 v[232:235], v[232:233], off
	s_nop 0
	v_lshl_add_u64 v[236:237], s[6:7], 0, v[58:59]
	global_load_dwordx4 v[240:243], v[236:237], off offset:16
	s_nop 0
	global_load_dwordx4 v[236:239], v[236:237], off
	s_nop 0
.Lmy_p5_noload:
	s_cmpk_gt_i32 s12, 0x3fff
	v_lshlrev_b32_e32 v68, 16, v91
	v_and_b32_e32 v69, 0xffff0000, v91
	v_lshlrev_b32_e32 v70, 16, v95
	v_and_b32_e32 v71, 0xffff0000, v95
	v_lshlrev_b32_e32 v74, 16, v90
	v_and_b32_e32 v75, 0xffff0000, v90
	v_lshlrev_b32_e32 v76, 16, v94
	v_and_b32_e32 v77, 0xffff0000, v94
	v_pk_add_f32 v[68:69], v[68:69], v[70:71]
	v_and_b32_e32 v71, 0xffff0000, v52
	v_lshlrev_b32_e32 v72, 16, v99
	v_and_b32_e32 v73, 0xffff0000, v99
	v_pk_add_f32 v[74:75], v[74:75], v[76:77]
	v_lshlrev_b32_e32 v70, 16, v52
	v_and_b32_e32 v77, 0xffff0000, v51
	v_mul_f32_e32 v52, 0xbfb8aa3b, v71
	v_pk_add_f32 v[68:69], v[68:69], v[72:73]
	v_mul_f32_e32 v73, 0xbfb8aa3b, v77
	v_exp_f32_e32 v52, v52
	v_lshlrev_b32_e32 v78, 16, v98
	v_and_b32_e32 v79, 0xffff0000, v98
	v_lshlrev_b32_e32 v80, 16, v89
	v_and_b32_e32 v81, 0xffff0000, v89
	v_lshlrev_b32_e32 v98, 16, v88
	v_exp_f32_e32 v73, v73
	v_and_b32_e32 v99, 0xffff0000, v88
	v_lshlrev_b32_e32 v88, 16, v92
	v_and_b32_e32 v89, 0xffff0000, v92
	v_lshlrev_b32_e32 v90, 16, v93
	v_and_b32_e32 v91, 0xffff0000, v93
	v_pk_add_f32 v[88:89], v[98:99], v[88:89]
	v_lshlrev_b32_e32 v92, 16, v96
	v_and_b32_e32 v93, 0xffff0000, v96
	v_pk_add_f32 v[88:89], v[88:89], v[92:93]
	v_lshlrev_b32_e32 v92, 16, v50
	v_lshlrev_b32_e32 v94, 16, v97
	v_and_b32_e32 v95, 0xffff0000, v97
	v_pk_add_f32 v[80:81], v[80:81], v[90:91]
	v_add_f32_e32 v52, 1.0, v52
	v_and_b32_e32 v93, 0xffff0000, v50
	v_mul_f32_e32 v50, 0xbfb8aa3b, v92
	v_pk_add_f32 v[74:75], v[74:75], v[78:79]
	v_pk_add_f32 v[78:79], v[80:81], v[94:95]
	v_add_f32_e32 v81, 1.0, v73
	v_rcp_f32_e32 v73, v52
	v_exp_f32_e32 v52, v50
	v_mul_f32_e32 v50, 0xbfb8aa3b, v93
	v_exp_f32_e32 v97, v50
	v_lshlrev_b32_e32 v98, 16, v111
	v_and_b32_e32 v99, 0xffff0000, v111
	v_lshlrev_b32_e32 v114, 16, v107
	v_and_b32_e32 v115, 0xffff0000, v107
	v_add_f32_e32 v52, 1.0, v52
	v_pk_add_f32 v[98:99], v[98:99], v[114:115]
	v_lshlrev_b32_e32 v114, 16, v103
	v_and_b32_e32 v115, 0xffff0000, v103
	v_rcp_f32_e32 v96, v52
	v_add_f32_e32 v52, 1.0, v97
	v_pk_add_f32 v[98:99], v[98:99], v[114:115]
	v_lshlrev_b32_e32 v114, 16, v57
	v_rcp_f32_e32 v97, v52
	v_and_b32_e32 v115, 0xffff0000, v57
	v_mul_f32_e32 v52, 0xbfb8aa3b, v114
	v_exp_f32_e32 v52, v52
	v_mul_f32_e32 v57, 0xbfb8aa3b, v115
	v_lshlrev_b32_e32 v120, 16, v110
	v_and_b32_e32 v121, 0xffff0000, v110
; __device__ __forceinline__ unsigned pk2(float lo, float hi) { const f32v2 v = {lo, hi}; return __builtin_bit_cast(unsigned, __builtin_convertvector(v, bf16v2)); }
; __global__ void __launch_bounds__(NTHREADS, 2) fwd(Args args) {
;     ...
;             for (int t2 = 0; t2 < 2; ++t2) { const int m = m0 + t2 * NGWc; if (m >= T) break;
;                 float o[16];
; #pragma unroll
;                 for (int j = 0; j < 2; ++j) { const unsigned a[4] = {ra[t2][j].x, ra[t2][j].y, ra[t2][j].z, ra[t2][j].w}, b2[4] = {rb[t2][j].x, rb[t2][j].y, rb[t2][j].z, rb[t2][j].w}, i3[4] = {ri[t2][j].x, ri[t2][j].y, ri[t2][j].z, ri[t2][j].w};
; #pragma unroll
;                     for (int q = 0; q < 4; ++q) { o[8 * j + 2 * q] = (bflo(a[q]) + bflo(b2[q])) + bflo(i3[q]); o[8 * j + 2 * q + 1] = (bfhi(a[q]) + bfhi(b2[q])) + bfhi(i3[q]); } }
;                 float ss = 0.f;
; #pragma unroll
;                 for (int j = 0; j < 16; ++j) ss += o[j] * o[j];
;                 ss += __shfl_xor(ss, 1); ss += __shfl_xor(ss, 2); ss += __shfl_xor(ss, 4); ss += __shfl_xor(ss, 8);
;                 const float rms = 1.f / sqrtf(ss * (1.f / 256.f) + RMS_EPS);
;                 const unsigned gw8[8] = {rg[t2][0].x, rg[t2][0].y, rg[t2][0].z, rg[t2][0].w, rg[t2][1].x, rg[t2][1].y, rg[t2][1].z, rg[t2][1].w};
;                 float r[16];
; #pragma unroll
;                 for (int j = 0; j < 8; ++j) { const float g0 = bflo(gw8[j]), g1 = bfhi(gw8[j]);
;                     r[2 * j] = o[2 * j] * rms * ng[2 * j] * g0 * __builtin_amdgcn_rcpf(1.f + __expf(-g0)); r[2 * j + 1] = o[2 * j + 1] * rms * ng[2 * j + 1] * g1 * __builtin_amdgcn_rcpf(1.f + __expf(-g1)); }
;                 u32x4 w0, w1; w0.x = pk2(r[0], r[1]); w0.y = pk2(r[2], r[3]); w0.z = pk2(r[4], r[5]); w0.w = pk2(r[6], r[7]);
;                 w1.x = pk2(r[8], r[9]); w1.y = pk2(r[10], r[11]); w1.z = pk2(r[12], r[13]); w1.w = pk2(r[14], r[15]);
;                 *(u32x4*)(ACAT + (size_t)m * D + 1024 + c0) = w0; *(u32x4*)(ACAT + (size_t)m * D + 1024 + c0 + 8) = w1; }
	v_lshlrev_b32_e32 v110, 16, v106
	v_and_b32_e32 v111, 0xffff0000, v106
	v_exp_f32_e32 v57, v57
	v_pk_add_f32 v[106:107], v[120:121], v[110:111]
	v_lshlrev_b32_e32 v120, 16, v109
	v_and_b32_e32 v121, 0xffff0000, v109
	v_lshlrev_b32_e32 v124, 16, v108
	v_and_b32_e32 v125, 0xffff0000, v108
	v_lshlrev_b32_e32 v108, 16, v104
	v_and_b32_e32 v109, 0xffff0000, v104
	v_lshlrev_b32_e32 v122, 16, v105
	v_and_b32_e32 v123, 0xffff0000, v105
	v_pk_add_f32 v[104:105], v[124:125], v[108:109]
	v_lshlrev_b32_e32 v108, 16, v100
	v_and_b32_e32 v109, 0xffff0000, v100
	v_pk_add_f32 v[120:121], v[120:121], v[122:123]
	v_lshlrev_b32_e32 v122, 16, v101
	v_and_b32_e32 v123, 0xffff0000, v101
	v_pk_add_f32 v[100:101], v[104:105], v[108:109]
	v_add_f32_e32 v52, 1.0, v52
	v_pk_add_f32 v[120:121], v[120:121], v[122:123]
	v_pk_mul_f32 v[104:105], v[100:101], v[100:101]
	v_lshlrev_b32_e32 v76, 16, v51
	v_mul_f32_e32 v51, 0xbfb8aa3b, v70
	v_rcp_f32_e32 v118, v52
	v_add_f32_e32 v52, 1.0, v57
	v_lshlrev_b32_e32 v110, 16, v102
	v_and_b32_e32 v111, 0xffff0000, v102
	v_pk_mul_f32 v[122:123], v[120:121], v[120:121]
	v_add_f32_e32 v57, v104, v105
	v_mul_f32_e32 v72, 0xbfb8aa3b, v76
	v_exp_f32_e32 v51, v51
	v_pk_add_f32 v[106:107], v[106:107], v[110:111]
	v_add_f32_e32 v57, v57, v122
	v_exp_f32_e32 v72, v72
	v_pk_mul_f32 v[110:111], v[106:107], v[106:107]
	v_add_f32_e32 v57, v57, v123
	v_add_f32_e32 v57, v57, v110
	v_pk_mul_f32 v[116:117], v[98:99], v[98:99]
	v_add_f32_e32 v57, v57, v111
	v_add_f32_e32 v51, 1.0, v51
	v_add_f32_e32 v57, v57, v116
	v_add_f32_e32 v80, 1.0, v72
	v_rcp_f32_e32 v72, v51
	v_pk_mul_f32 v[50:51], v[88:89], v[88:89]
	v_add_f32_e32 v57, v57, v117
	v_add_f32_e32 v50, v57, v50
	v_pk_mul_f32 v[112:113], v[78:79], v[78:79]
	v_lshlrev_b32_e32 v102, 16, v56
	v_add_f32_e32 v50, v50, v51
	v_rcp_f32_e32 v119, v52
	v_mul_f32_e32 v52, 0xbfb8aa3b, v102
	v_add_f32_e32 v50, v50, v112
	v_pk_mul_f32 v[94:95], v[74:75], v[74:75]
	v_exp_f32_e32 v52, v52
	v_add_f32_e32 v50, v50, v113
	v_add_f32_e32 v50, v50, v94
	v_pk_mul_f32 v[90:91], v[68:69], v[68:69]
	v_add_f32_e32 v50, v50, v95
	v_add_f32_e32 v50, v50, v90
	v_and_b32_e32 v103, 0xffff0000, v56
	v_add_f32_e32 v52, 1.0, v52
	v_add_f32_e32 v90, v50, v91
	v_rcp_f32_e32 v56, v52
	v_mul_f32_e32 v52, 0xbfb8aa3b, v103
	ds_bpermute_b32 v91, v82, v90
	v_exp_f32_e32 v52, v52
	v_and_b32_e32 v51, 0xffff0000, v55
	v_and_b32_e32 v95, 0xffff0000, v54
	v_mul_f32_e32 v104, 0xbfb8aa3b, v95
	v_add_f32_e32 v50, 1.0, v52
	s_waitcnt lgkmcnt(0)
	v_add_f32_e32 v52, v90, v91
	v_rcp_f32_e32 v57, v50
	v_lshlrev_b32_e32 v50, 16, v55
	ds_bpermute_b32 v55, v83, v52
	v_exp_f32_e32 v104, v104
	v_lshlrev_b32_e32 v94, 16, v54
	v_mul_f32_e32 v54, 0xbfb8aa3b, v94
	v_exp_f32_e32 v54, v54
	s_waitcnt lgkmcnt(0)
	v_add_f32_e32 v52, v52, v55
	ds_bpermute_b32 v55, v84, v52
	v_mul_f32_e32 v90, 0xbfb8aa3b, v50
	v_mul_f32_e32 v91, 0xbfb8aa3b, v51
	v_exp_f32_e32 v90, v90
	v_exp_f32_e32 v91, v91
	s_waitcnt lgkmcnt(0)
	v_add_f32_e32 v52, v52, v55
	ds_bpermute_b32 v55, v85, v52
	v_add_f32_e32 v54, 1.0, v54
	v_rcp_f32_e32 v54, v54
	v_add_f32_e32 v90, 1.0, v90
	v_add_f32_e32 v91, 1.0, v91
	s_waitcnt lgkmcnt(0)
	v_add_f32_e32 v52, v52, v55
	v_fmamk_f32 v52, v52, 0x3b800000, v86
	v_mul_f32_e32 v55, 0x4f800000, v52
	v_cmp_gt_f32_e32 vcc, s21, v52
	v_rcp_f32_e32 v90, v90
	v_rcp_f32_e32 v91, v91
	v_cndmask_b32_e32 v52, v52, v55, vcc
	v_sqrt_f32_e32 v55, v52
	v_rcp_f32_e32 v80, v80
	v_rcp_f32_e32 v81, v81
	v_add_u32_e32 v105, -1, v55
	v_fma_f32 v108, -v105, v55, v52
	v_cmp_ge_f32_e64 s[6:7], 0, v108
	v_add_u32_e32 v108, 1, v55
	s_nop 0
	v_cndmask_b32_e64 v105, v55, v105, s[6:7]
	v_fma_f32 v55, -v108, v55, v52
	v_cmp_lt_f32_e64 s[6:7], 0, v55
	s_nop 1
	v_cndmask_b32_e64 v55, v105, v108, s[6:7]
	v_mul_f32_e32 v105, 0x37800000, v55
	v_cndmask_b32_e32 v55, v55, v105, vcc
	v_cmp_class_f32_e32 vcc, v52, v87
	s_nop 1
	v_cndmask_b32_e32 v52, v55, v52, vcc
	v_div_scale_f32 v105, s[6:7], v52, v52, 1.0
	v_rcp_f32_e32 v108, v105
	v_add_f32_e32 v55, 1.0, v104
	v_rcp_f32_e32 v55, v55
	v_fma_f32 v104, -v105, v108, 1.0
	v_fmac_f32_e32 v108, v104, v108
	v_div_scale_f32 v104, vcc, 1.0, v52, 1.0
	v_mul_f32_e32 v109, v104, v108
	v_fma_f32 v110, -v105, v109, v104
	v_fmac_f32_e32 v109, v110, v108
	v_fma_f32 v104, -v105, v109, v104
	v_div_fmas_f32 v104, v104, v108, v109
	v_div_fixup_f32 v52, v104, v52, 1.0
	v_pk_mul_f32 v[100:101], v[52:53], v[100:101] op_sel_hi:[0,1]
	v_pk_mul_f32 v[100:101], v[100:101], v[2:3]
	s_nop 0
	v_pk_mul_f32 v[94:95], v[100:101], v[94:95]
	s_nop 0
	v_pk_mul_f32 v[54:55], v[94:95], v[54:55]
	v_pk_mul_f32 v[94:95], v[52:53], v[120:121] op_sel_hi:[0,1]
	v_pk_mul_f32 v[94:95], v[94:95], v[4:5]
	s_nop 0
	v_pk_mul_f32 v[50:51], v[94:95], v[50:51]
	s_nop 0
	v_pk_mul_f32 v[90:91], v[50:51], v[90:91]
	v_pk_mul_f32 v[50:51], v[52:53], v[106:107] op_sel_hi:[0,1]
	v_pk_mul_f32 v[50:51], v[50:51], v[6:7]
	s_nop 0
	v_pk_mul_f32 v[50:51], v[50:51], v[102:103]
	s_nop 0
	v_pk_mul_f32 v[56:57], v[50:51], v[56:57]
	v_pk_mul_f32 v[50:51], v[52:53], v[98:99] op_sel_hi:[0,1]
	v_pk_mul_f32 v[50:51], v[50:51], v[8:9]
	s_nop 0
	v_pk_mul_f32 v[50:51], v[50:51], v[114:115]
	s_nop 0
	v_pk_mul_f32 v[94:95], v[50:51], v[118:119]
	v_pk_mul_f32 v[50:51], v[52:53], v[88:89] op_sel_hi:[0,1]
	v_pk_mul_f32 v[50:51], v[50:51], v[10:11]
	s_nop 0
	v_pk_mul_f32 v[50:51], v[50:51], v[92:93]
	s_nop 0
	v_pk_mul_f32 v[88:89], v[50:51], v[96:97]
	v_pk_mul_f32 v[50:51], v[52:53], v[78:79] op_sel_hi:[0,1]
	v_pk_mul_f32 v[50:51], v[50:51], v[12:13]
	s_nop 0
	v_pk_mul_f32 v[50:51], v[50:51], v[76:77]
	s_nop 0
	v_pk_mul_f32 v[76:77], v[50:51], v[80:81]
	v_pk_mul_f32 v[50:51], v[52:53], v[74:75] op_sel_hi:[0,1]
	v_pk_mul_f32 v[50:51], v[50:51], v[14:15]
	s_nop 0
	v_pk_mul_f32 v[50:51], v[50:51], v[70:71]
	v_lshlrev_b32_e32 v70, 16, v53
	v_and_b32_e32 v71, 0xffff0000, v53
	v_mul_f32_e32 v53, 0xbfb8aa3b, v70
	v_mul_f32_e32 v74, 0xbfb8aa3b, v71
	v_exp_f32_e32 v53, v53
	v_exp_f32_e32 v74, v74
	v_pk_mul_f32 v[72:73], v[50:51], v[72:73]
	v_add_f32_e32 v50, 1.0, v53
	v_add_f32_e32 v51, 1.0, v74
	v_rcp_f32_e32 v50, v50
	v_rcp_f32_e32 v51, v51
	v_pk_mul_f32 v[52:53], v[52:53], v[68:69] op_sel_hi:[0,1]
	v_pk_mul_f32 v[52:53], v[52:53], v[16:17]
	s_nop 0
	v_pk_mul_f32 v[52:53], v[52:53], v[70:71]
	s_nop 0
	v_pk_mul_f32 v[68:69], v[52:53], v[50:51]
	v_cvt_pk_bf16_f32 v50, v54, v55
	v_cvt_pk_bf16_f32 v51, v90, v91
	v_cvt_pk_bf16_f32 v52, v56, v57
	v_cvt_pk_bf16_f32 v53, v94, v95
	v_cvt_pk_bf16_f32 v57, v68, v69
	v_lshl_add_u64 v[68:69], v[66:67], 0, s[14:15]
	v_cvt_pk_bf16_f32 v54, v88, v89
	v_cvt_pk_bf16_f32 v55, v76, v77
	v_cvt_pk_bf16_f32 v56, v72, v73
	global_store_dwordx4 v[68:69], v[50:53], off offset:2048
	global_store_dwordx4 v[68:69], v[54:57], off offset:2064
	s_cbranch_scc1 .LBB0_597
; __global__ void __launch_bounds__(NTHREADS, 2) fwd(Args args) {
;     ...
;             for (int t2 = 0; t2 < 2; ++t2) { const int m = m0 + t2 * NGWc; if (m >= T) break;
;                 float o[16];
; #pragma unroll
;                 for (int j = 0; j < 2; ++j) { const unsigned a[4] = {ra[t2][j].x, ra[t2][j].y, ra[t2][j].z, ra[t2][j].w}, b2[4] = {rb[t2][j].x, rb[t2][j].y, rb[t2][j].z, rb[t2][j].w}, i3[4] = {ri[t2][j].x, ri[t2][j].y, ri[t2][j].z, ri[t2][j].w};
; #pragma unroll
;                     for (int q = 0; q < 4; ++q) { o[8 * j + 2 * q] = (bflo(a[q]) + bflo(b2[q])) + bflo(i3[q]); o[8 * j + 2 * q + 1] = (bfhi(a[q]) + bfhi(b2[q])) + bfhi(i3[q]); } }
;                 float ss = 0.f;
; #pragma unroll
;                 for (int j = 0; j < 16; ++j) ss += o[j] * o[j];
;                 ss += __shfl_xor(ss, 1); ss += __shfl_xor(ss, 2); ss += __shfl_xor(ss, 4); ss += __shfl_xor(ss, 8);
;                 const float rms = 1.f / sqrtf(ss * (1.f / 256.f) + RMS_EPS);
;                 const unsigned gw8[8] = {rg[t2][0].x, rg[t2][0].y, rg[t2][0].z, rg[t2][0].w, rg[t2][1].x, rg[t2][1].y, rg[t2][1].z, rg[t2][1].w};
;                 float r[16];
; #pragma unroll
;                 for (int j = 0; j < 8; ++j) { const float g0 = bflo(gw8[j]), g1 = bfhi(gw8[j]);
;                     r[2 * j] = o[2 * j] * rms * ng[2 * j] * g0 * __builtin_amdgcn_rcpf(1.f + __expf(-g0)); r[2 * j + 1] = o[2 * j + 1] * rms * ng[2 * j + 1] * g1 * __builtin_amdgcn_rcpf(1.f + __expf(-g1)); }
	v_lshlrev_b32_e32 v50, 16, v49
	v_and_b32_e32 v51, 0xffff0000, v49
	v_lshlrev_b32_e32 v52, 16, v45
	v_and_b32_e32 v53, 0xffff0000, v45
	v_pk_add_f32 v[50:51], v[50:51], v[52:53]
	v_lshlrev_b32_e32 v52, 16, v41
	v_and_b32_e32 v53, 0xffff0000, v41
	v_pk_add_f32 v[50:51], v[50:51], v[52:53]
	v_lshlrev_b32_e32 v52, 16, v48
	v_and_b32_e32 v53, 0xffff0000, v48
	v_lshlrev_b32_e32 v48, 16, v44
	v_and_b32_e32 v49, 0xffff0000, v44
	v_pk_add_f32 v[44:45], v[52:53], v[48:49]
	v_lshlrev_b32_e32 v48, 16, v40
	v_and_b32_e32 v49, 0xffff0000, v40
	v_pk_add_f32 v[44:45], v[44:45], v[48:49]
	v_lshlrev_b32_e32 v48, 16, v20
	v_and_b32_e32 v49, 0xffff0000, v20
	v_mul_f32_e32 v20, 0xbfb8aa3b, v48
	v_exp_f32_e32 v20, v20
	v_mul_f32_e32 v40, 0xbfb8aa3b, v49
	v_exp_f32_e32 v41, v40
	v_lshlrev_b32_e32 v52, 16, v47
	v_and_b32_e32 v53, 0xffff0000, v47
	v_lshlrev_b32_e32 v54, 16, v43
	v_and_b32_e32 v55, 0xffff0000, v43
	v_pk_add_f32 v[52:53], v[52:53], v[54:55]
	v_lshlrev_b32_e32 v54, 16, v39
	v_and_b32_e32 v55, 0xffff0000, v39
	v_add_f32_e32 v20, 1.0, v20
	v_pk_add_f32 v[52:53], v[52:53], v[54:55]
	v_lshlrev_b32_e32 v54, 16, v19
	v_rcp_f32_e32 v40, v20
	v_add_f32_e32 v20, 1.0, v41
	v_and_b32_e32 v55, 0xffff0000, v19
	v_mul_f32_e32 v19, 0xbfb8aa3b, v54
	v_rcp_f32_e32 v41, v20
	v_exp_f32_e32 v19, v19
	v_mul_f32_e32 v20, 0xbfb8aa3b, v55
	v_exp_f32_e32 v20, v20
	v_lshlrev_b32_e32 v74, 16, v46
	v_and_b32_e32 v75, 0xffff0000, v46
	v_lshlrev_b32_e32 v46, 16, v42
	v_and_b32_e32 v47, 0xffff0000, v42
	v_pk_add_f32 v[42:43], v[74:75], v[46:47]
	v_lshlrev_b32_e32 v46, 16, v38
	v_and_b32_e32 v47, 0xffff0000, v38
	v_pk_add_f32 v[38:39], v[42:43], v[46:47]
	v_lshlrev_b32_e32 v42, 16, v18
	v_add_f32_e32 v19, 1.0, v19
	v_and_b32_e32 v43, 0xffff0000, v18
	v_mul_f32_e32 v18, 0xbfb8aa3b, v42
	v_rcp_f32_e32 v56, v19
	v_add_f32_e32 v19, 1.0, v20
	v_exp_f32_e32 v20, v18
	v_mul_f32_e32 v18, 0xbfb8aa3b, v43
	v_exp_f32_e32 v47, v18
	v_lshlrev_b32_e32 v74, 16, v37
	v_and_b32_e32 v75, 0xffff0000, v37
	v_lshlrev_b32_e32 v76, 16, v33
	v_and_b32_e32 v77, 0xffff0000, v33
	v_add_f32_e32 v20, 1.0, v20
	v_pk_add_f32 v[74:75], v[74:75], v[76:77]
	v_lshlrev_b32_e32 v76, 16, v29
	v_and_b32_e32 v77, 0xffff0000, v29
	v_rcp_f32_e32 v46, v20
	v_add_f32_e32 v20, 1.0, v47
	v_pk_add_f32 v[74:75], v[74:75], v[76:77]
	v_lshlrev_b32_e32 v76, 16, v25
	v_rcp_f32_e32 v47, v20
	v_and_b32_e32 v77, 0xffff0000, v25
	v_mul_f32_e32 v20, 0xbfb8aa3b, v76
	v_exp_f32_e32 v20, v20
	v_mul_f32_e32 v25, 0xbfb8aa3b, v77
	v_lshlrev_b32_e32 v88, 16, v36
	v_and_b32_e32 v89, 0xffff0000, v36
	v_lshlrev_b32_e32 v36, 16, v32
	v_and_b32_e32 v37, 0xffff0000, v32
	v_exp_f32_e32 v25, v25
	v_pk_add_f32 v[32:33], v[88:89], v[36:37]
	v_lshlrev_b32_e32 v88, 16, v35
	v_and_b32_e32 v89, 0xffff0000, v35
	v_lshlrev_b32_e32 v92, 16, v34
	v_and_b32_e32 v93, 0xffff0000, v34
	v_lshlrev_b32_e32 v34, 16, v30
	v_and_b32_e32 v35, 0xffff0000, v30
	v_lshlrev_b32_e32 v90, 16, v31
	v_and_b32_e32 v91, 0xffff0000, v31
	v_pk_add_f32 v[30:31], v[92:93], v[34:35]
	v_lshlrev_b32_e32 v34, 16, v26
	v_and_b32_e32 v35, 0xffff0000, v26
	v_pk_add_f32 v[88:89], v[88:89], v[90:91]
	v_lshlrev_b32_e32 v90, 16, v27
	v_and_b32_e32 v91, 0xffff0000, v27
	v_pk_add_f32 v[26:27], v[30:31], v[34:35]
	v_add_f32_e32 v20, 1.0, v20
	v_pk_add_f32 v[88:89], v[88:89], v[90:91]
	v_pk_mul_f32 v[30:31], v[26:27], v[26:27]
	v_rcp_f32_e32 v80, v20
	v_add_f32_e32 v20, 1.0, v25
	v_lshlrev_b32_e32 v36, 16, v28
	v_and_b32_e32 v37, 0xffff0000, v28
	v_pk_mul_f32 v[90:91], v[88:89], v[88:89]
	v_add_f32_e32 v25, v30, v31
	v_pk_add_f32 v[32:33], v[32:33], v[36:37]
	v_add_f32_e32 v25, v25, v90
	v_pk_mul_f32 v[36:37], v[32:33], v[32:33]
	v_add_f32_e32 v25, v25, v91
	v_add_f32_e32 v25, v25, v36
	v_pk_mul_f32 v[78:79], v[74:75], v[74:75]
	v_add_f32_e32 v25, v25, v37
	v_add_f32_e32 v25, v25, v78
	v_rcp_f32_e32 v57, v19
	v_pk_mul_f32 v[18:19], v[38:39], v[38:39]
	v_add_f32_e32 v25, v25, v79
	v_add_f32_e32 v18, v25, v18
	v_pk_mul_f32 v[72:73], v[52:53], v[52:53]
	v_lshlrev_b32_e32 v28, 16, v24
	v_add_f32_e32 v18, v18, v19
	v_rcp_f32_e32 v81, v20
	v_mul_f32_e32 v20, 0xbfb8aa3b, v28
	v_add_f32_e32 v18, v18, v72
	v_pk_mul_f32 v[70:71], v[44:45], v[44:45]
	v_exp_f32_e32 v20, v20
	v_add_f32_e32 v18, v18, v73
	v_add_f32_e32 v18, v18, v70
	v_pk_mul_f32 v[68:69], v[50:51], v[50:51]
	v_add_f32_e32 v18, v18, v71
	v_add_f32_e32 v18, v18, v68
	v_and_b32_e32 v29, 0xffff0000, v24
	v_add_f32_e32 v20, 1.0, v20
	v_add_f32_e32 v30, v18, v69
	v_rcp_f32_e32 v24, v20
	v_mul_f32_e32 v20, 0xbfb8aa3b, v29
	ds_bpermute_b32 v31, v82, v30
	v_exp_f32_e32 v20, v20
	v_and_b32_e32 v19, 0xffff0000, v23
	v_and_b32_e32 v35, 0xffff0000, v22
	v_mul_f32_e32 v36, 0xbfb8aa3b, v35
	v_add_f32_e32 v18, 1.0, v20
	s_waitcnt lgkmcnt(0)
; __device__ __forceinline__ unsigned pk2(float lo, float hi) { const f32v2 v = {lo, hi}; return __builtin_bit_cast(unsigned, __builtin_convertvector(v, bf16v2)); }
; __global__ void __launch_bounds__(NTHREADS, 2) fwd(Args args) {
;     ...
;                 float ss = 0.f;
; #pragma unroll
;                 for (int j = 0; j < 16; ++j) ss += o[j] * o[j];
;                 ss += __shfl_xor(ss, 1); ss += __shfl_xor(ss, 2); ss += __shfl_xor(ss, 4); ss += __shfl_xor(ss, 8);
;                 const float rms = 1.f / sqrtf(ss * (1.f / 256.f) + RMS_EPS);
;                 const unsigned gw8[8] = {rg[t2][0].x, rg[t2][0].y, rg[t2][0].z, rg[t2][0].w, rg[t2][1].x, rg[t2][1].y, rg[t2][1].z, rg[t2][1].w};
;                 float r[16];
; #pragma unroll
;                 for (int j = 0; j < 8; ++j) { const float g0 = bflo(gw8[j]), g1 = bfhi(gw8[j]);
;                     r[2 * j] = o[2 * j] * rms * ng[2 * j] * g0 * __builtin_amdgcn_rcpf(1.f + __expf(-g0)); r[2 * j + 1] = o[2 * j + 1] * rms * ng[2 * j + 1] * g1 * __builtin_amdgcn_rcpf(1.f + __expf(-g1)); }
;                 u32x4 w0, w1; w0.x = pk2(r[0], r[1]); w0.y = pk2(r[2], r[3]); w0.z = pk2(r[4], r[5]); w0.w = pk2(r[6], r[7]);
;                 w1.x = pk2(r[8], r[9]); w1.y = pk2(r[10], r[11]); w1.z = pk2(r[12], r[13]); w1.w = pk2(r[14], r[15]);
;                 *(u32x4*)(ACAT + (size_t)m * D + 1024 + c0) = w0; *(u32x4*)(ACAT + (size_t)m * D + 1024 + c0 + 8) = w1; }
	v_add_f32_e32 v20, v30, v31
	v_rcp_f32_e32 v25, v18
	v_lshlrev_b32_e32 v18, 16, v23
	ds_bpermute_b32 v23, v83, v20
	v_exp_f32_e32 v36, v36
	v_lshlrev_b32_e32 v34, 16, v22
	v_mul_f32_e32 v22, 0xbfb8aa3b, v34
	v_exp_f32_e32 v22, v22
	s_waitcnt lgkmcnt(0)
	v_add_f32_e32 v20, v20, v23
	ds_bpermute_b32 v23, v84, v20
	v_mul_f32_e32 v30, 0xbfb8aa3b, v18
	v_mul_f32_e32 v31, 0xbfb8aa3b, v19
	v_exp_f32_e32 v30, v30
	v_exp_f32_e32 v31, v31
	s_waitcnt lgkmcnt(0)
	v_add_f32_e32 v20, v20, v23
	ds_bpermute_b32 v23, v85, v20
	v_add_f32_e32 v22, 1.0, v22
	v_rcp_f32_e32 v22, v22
	v_add_f32_e32 v30, 1.0, v30
	v_add_f32_e32 v31, 1.0, v31
	s_waitcnt lgkmcnt(0)
	v_add_f32_e32 v20, v20, v23
	v_fmamk_f32 v20, v20, 0x3b800000, v86
	v_mul_f32_e32 v23, 0x4f800000, v20
	v_cmp_gt_f32_e32 vcc, s21, v20
	v_rcp_f32_e32 v30, v30
	v_rcp_f32_e32 v31, v31
	v_cndmask_b32_e32 v20, v20, v23, vcc
	v_sqrt_f32_e32 v23, v20
	s_ashr_i32 s13, s12, 31
	v_add_u32_e32 v37, -1, v23
	v_fma_f32 v68, -v37, v23, v20
	v_cmp_ge_f32_e64 s[6:7], 0, v68
	v_add_u32_e32 v68, 1, v23
	s_nop 0
	v_cndmask_b32_e64 v37, v23, v37, s[6:7]
	v_fma_f32 v23, -v68, v23, v20
	v_cmp_lt_f32_e64 s[6:7], 0, v23
	s_nop 1
	v_cndmask_b32_e64 v23, v37, v68, s[6:7]
	v_mul_f32_e32 v37, 0x37800000, v23
	v_cndmask_b32_e32 v23, v23, v37, vcc
	v_cmp_class_f32_e32 vcc, v20, v87
	s_nop 1
	v_cndmask_b32_e32 v20, v23, v20, vcc
	v_div_scale_f32 v37, s[6:7], v20, v20, 1.0
	v_rcp_f32_e32 v68, v37
	v_add_f32_e32 v23, 1.0, v36
	v_rcp_f32_e32 v23, v23
	s_lshl_b64 s[6:7], s[12:13], 12
	v_fma_f32 v36, -v37, v68, 1.0
	v_fmac_f32_e32 v68, v36, v68
	v_div_scale_f32 v36, vcc, 1.0, v20, 1.0
	v_mul_f32_e32 v69, v36, v68
	v_fma_f32 v70, -v37, v69, v36
	v_fmac_f32_e32 v69, v70, v68
	v_fma_f32 v36, -v37, v69, v36
	v_div_fmas_f32 v36, v36, v68, v69
	v_div_fixup_f32 v20, v36, v20, 1.0
	v_pk_mul_f32 v[26:27], v[20:21], v[26:27] op_sel_hi:[0,1]
	v_pk_mul_f32 v[26:27], v[26:27], v[2:3]
	s_nop 0
	v_pk_mul_f32 v[26:27], v[26:27], v[34:35]
	v_lshlrev_b32_e32 v34, 16, v21
	v_pk_mul_f32 v[22:23], v[26:27], v[22:23]
	v_pk_mul_f32 v[26:27], v[20:21], v[88:89] op_sel_hi:[0,1]
	v_pk_mul_f32 v[26:27], v[26:27], v[4:5]
	v_and_b32_e32 v35, 0xffff0000, v21
	v_pk_mul_f32 v[18:19], v[26:27], v[18:19]
	v_mul_f32_e32 v36, 0xbfb8aa3b, v35
	v_pk_mul_f32 v[26:27], v[18:19], v[30:31]
	v_pk_mul_f32 v[18:19], v[20:21], v[32:33] op_sel_hi:[0,1]
	v_pk_mul_f32 v[18:19], v[18:19], v[6:7]
	s_nop 0
	v_pk_mul_f32 v[18:19], v[18:19], v[28:29]
	s_nop 0
	v_pk_mul_f32 v[24:25], v[18:19], v[24:25]
	v_pk_mul_f32 v[18:19], v[20:21], v[74:75] op_sel_hi:[0,1]
	v_pk_mul_f32 v[18:19], v[18:19], v[8:9]
	s_nop 0
	v_pk_mul_f32 v[18:19], v[18:19], v[76:77]
	s_nop 0
	v_pk_mul_f32 v[28:29], v[18:19], v[80:81]
	v_pk_mul_f32 v[18:19], v[20:21], v[38:39] op_sel_hi:[0,1]
	v_pk_mul_f32 v[18:19], v[18:19], v[10:11]
	v_exp_f32_e32 v38, v36
	v_pk_mul_f32 v[18:19], v[18:19], v[42:43]
	s_nop 0
	v_pk_mul_f32 v[30:31], v[18:19], v[46:47]
	v_pk_mul_f32 v[18:19], v[20:21], v[52:53] op_sel_hi:[0,1]
	v_pk_mul_f32 v[18:19], v[18:19], v[12:13]
	s_nop 0
	v_pk_mul_f32 v[18:19], v[18:19], v[54:55]
	s_nop 0
	v_pk_mul_f32 v[32:33], v[18:19], v[56:57]
	v_pk_mul_f32 v[18:19], v[20:21], v[44:45] op_sel_hi:[0,1]
	v_mul_f32_e32 v21, 0xbfb8aa3b, v34
	v_exp_f32_e32 v21, v21
	v_pk_mul_f32 v[18:19], v[18:19], v[14:15]
	s_nop 0
	v_pk_mul_f32 v[18:19], v[18:19], v[48:49]
	s_nop 0
	v_pk_mul_f32 v[36:37], v[18:19], v[40:41]
	v_add_f32_e32 v18, 1.0, v21
	v_add_f32_e32 v19, 1.0, v38
	v_rcp_f32_e32 v18, v18
	v_rcp_f32_e32 v19, v19
	v_pk_mul_f32 v[20:21], v[20:21], v[50:51] op_sel_hi:[0,1]
	v_pk_mul_f32 v[20:21], v[20:21], v[16:17]
	s_nop 0
	v_pk_mul_f32 v[20:21], v[20:21], v[34:35]
	s_nop 0
	v_pk_mul_f32 v[34:35], v[20:21], v[18:19]
	v_cvt_pk_bf16_f32 v18, v22, v23
	v_cvt_pk_bf16_f32 v19, v26, v27
	v_cvt_pk_bf16_f32 v20, v24, v25
	v_cvt_pk_bf16_f32 v21, v28, v29
	v_lshl_add_u64 v[26:27], v[66:67], 0, s[6:7]
	v_cvt_pk_bf16_f32 v22, v30, v31
	v_cvt_pk_bf16_f32 v23, v32, v33
	v_cvt_pk_bf16_f32 v24, v36, v37
	v_cvt_pk_bf16_f32 v25, v34, v35
	global_store_dwordx4 v[26:27], v[18:21], off offset:2048
	global_store_dwordx4 v[26:27], v[22:25], off offset:2064
	s_branch .LBB0_597
